# baseline (speedup 1.0000x reference)
.LBB2_12:
	v_max3_f32 v69, v46, v47, v48
	s_and_b64 vcc, exec, s[38:39]
	s_nop 1
	v_max3_f32 v69, v69, v49, v42
	v_max3_f32 v69, v69, v43, v44
	v_max3_f32 v69, v69, v45, v38
	v_max3_f32 v69, v69, v39, v40
	v_max3_f32 v69, v69, v41, v34
	v_max3_f32 v69, v69, v35, v36
	v_max_f32_e32 v69, v69, v37
	v_mov_b32_e32 v71, v69
	s_nop 1
	v_permlane16_swap_b32_e32 v69, v71
	v_max_f32_e32 v69, v69, v71
	v_mov_b32_e32 v71, v69
	s_nop 1
	v_permlane32_swap_b32_e32 v69, v71
	v_max_f32_e32 v69, v69, v71
	s_sleep 4
	s_cbranch_vccnz .Lattn_first_tile
	v_cmp_lt_f32_e32 vcc, s58, v69
	s_nop 1
	s_cbranch_vccz .LBB2_5
	v_max_f32_e32 v71, v69, v69
	v_max_f32_e32 v80, 0, v71
	s_branch .Lattn_rescale
